# MoE tile loops (P9, P10): owner-expert search vectorized (lane k reads tstart[k], popcount of the compare mask) instead of 8 LDS round trips of readfirstlane/compare chains
# speedup vs baseline: 1.0201x; 1.0087x over previous
.LBB0_1152:
	s_add_i32 s34, s34, 1
	s_mul_i32 s2, s34, s84
	s_add_i32 s2, s2, s87
	s_cmp_lt_i32 s2, s24
	s_cselect_b64 s[10:11], -1, 0
	s_cmp_ge_i32 s2, s24
	s_cbranch_scc1 .LBB0_1154
	s_ashr_i32 s3, s2, 31
	s_lshr_b32 s3, s3, 29
	s_add_i32 s3, s2, s3
	s_ashr_i32 s22, s3, 3
	s_and_b32 s3, s3, -8
	s_sub_i32 s2, s2, s3
	v_mov_b32_e32 v133, s2
	v_alignbit_b32 v133, s21, v133, 31
	v_mov_b32_e32 v138, s47
	v_readfirstlane_b32 s3, v133
	s_mul_i32 s2, s3, s2
	s_add_i32 s2, s2, s22
	s_ashr_i32 s3, s2, 31
	s_lshr_b32 s3, s3, 25
	s_add_i32 s3, s2, s3
	s_ashr_i32 s22, s3, 7
	s_lshl_b32 s22, s22, 3
	s_sub_i32 s23, s21, s22
	s_min_i32 s23, s23, 8
	s_abs_i32 s62, s23
	v_cvt_f32_u32_e32 v133, s62
	s_sub_i32 s64, 0, s62
	s_and_b32 s3, s3, 0xffffff80
	s_sub_i32 s2, s2, s3
	v_rcp_iflag_f32_e32 v133, v133
	s_abs_i32 s3, s2
	s_xor_b32 s63, s2, s23
	s_ashr_i32 s63, s63, 31
	v_mul_f32_e32 v133, 0x4f7ffffe, v133
	v_cvt_u32_f32_e32 v133, v133
	v_mov_b32_e32 v140, s48
	v_readfirstlane_b32 s67, v133
	s_mul_i32 s64, s64, s67
	s_mul_hi_u32 s64, s67, s64
	s_add_i32 s67, s67, s64
	s_mul_hi_u32 s64, s3, s67
	s_mul_i32 s67, s64, s62
	s_sub_i32 s3, s3, s67
	s_add_i32 s68, s64, 1
	s_sub_i32 s67, s3, s62
	s_cmp_ge_u32 s3, s62
	s_cselect_b32 s64, s68, s64
	s_cselect_b32 s3, s67, s3
	s_add_i32 s67, s64, 1
	s_cmp_ge_u32 s3, s62
	s_cselect_b32 s3, s67, s64
	s_xor_b32 s3, s3, s63
	s_sub_i32 s62, s3, s63
	s_mul_i32 s3, s62, s23
	s_sub_i32 s2, s2, s3
	s_add_i32 s2, s2, s22
	v_mbcnt_lo_u32_b32 v133, -1, 0
	v_mbcnt_hi_u32_b32 v133, -1, v133
	v_lshlrev_b32_e32 v133, 2, v133
	v_add_u32_e32 v133, 0x20080, v133
	ds_read_b32 v134, v133
	s_waitcnt lgkmcnt(0)
	v_cmp_ge_i32_e32 vcc, s2, v134
	s_nop 1
	s_and_b32 s3, vcc_lo, -2
	s_bcnt1_i32_b32 s3, s3
	v_mov_b32_e32 v146, s3
	v_lshlrev_b32_e32 v133, 2, v146
	v_add_u32_e32 v133, 0, v133
	v_add_u32_e32 v134, 0x20080, v133
	ds_read2_b32 v[134:135], v134 offset1:33
	v_add_u32_e32 v133, 0x20000, v133
	ds_read_b32 v133, v133
	s_waitcnt lgkmcnt(1)
	v_readfirstlane_b32 s3, v134
	s_sub_i32 s2, s2, s3
	s_lshl_b32 s22, s2, 8
	s_waitcnt lgkmcnt(0)
	v_readfirstlane_b32 s2, v133
	s_sub_i32 s2, s2, s22
	s_min_i32 s63, s2, 0x100
	v_readfirstlane_b32 s2, v135
	s_add_i32 s64, s2, s22

.LBB0_1249:
	s_add_i32 s50, s50, 1
	s_mul_i32 s2, s50, s84
	s_add_i32 s2, s2, s87
	s_cmp_lt_i32 s2, s41
	s_cselect_b64 s[4:5], -1, 0
	s_cmp_ge_i32 s2, s41
	s_cbranch_scc1 .LBB0_1251
	s_ashr_i32 s3, s2, 31
	s_lshr_b32 s3, s3, 29
	s_add_i32 s3, s2, s3
	s_ashr_i32 s7, s3, 3
	s_and_b32 s3, s3, -8
	s_sub_i32 s2, s2, s3
	s_lshr_b32 s3, s2, 31
	s_add_i32 s3, s3, s33
	s_mul_i32 s2, s3, s2
	s_add_i32 s2, s2, s7
	s_ashr_i32 s3, s2, 31
	s_lshr_b32 s3, s3, 25
	s_add_i32 s3, s2, s3
	s_ashr_i32 s7, s3, 7
	s_lshl_b32 s7, s7, 4
	s_sub_i32 s8, s33, s7
	s_min_i32 s8, s8, 16
	s_abs_i32 s9, s8
	v_cvt_f32_u32_e32 v132, s9
	s_sub_i32 s11, 0, s9
	s_and_b32 s3, s3, 0xffffff80
	s_sub_i32 s2, s2, s3
	v_rcp_iflag_f32_e32 v132, v132
	s_abs_i32 s3, s2
	s_xor_b32 s10, s2, s8
	s_ashr_i32 s10, s10, 31
	v_mul_f32_e32 v132, 0x4f7ffffe, v132
	v_cvt_u32_f32_e32 v132, v132
	v_mov_b32_e32 v134, s60
	v_mov_b32_e32 v136, s61
	v_mov_b32_e32 v138, s62
	v_readfirstlane_b32 s12, v132
	s_mul_i32 s11, s11, s12
	s_mul_hi_u32 s11, s12, s11
	s_add_i32 s12, s12, s11
	s_mul_hi_u32 s11, s3, s12
	s_mul_i32 s12, s11, s9
	s_sub_i32 s3, s3, s12
	s_add_i32 s13, s11, 1
	s_sub_i32 s12, s3, s9
	s_cmp_ge_u32 s3, s9
	s_cselect_b32 s11, s13, s11
	s_cselect_b32 s3, s12, s3
	s_add_i32 s12, s11, 1
	s_cmp_ge_u32 s3, s9
	s_cselect_b32 s3, s12, s11
	s_xor_b32 s3, s3, s10
	s_sub_i32 s76, s3, s10
	s_mul_i32 s3, s76, s8
	s_sub_i32 s2, s2, s3
	s_add_i32 s2, s2, s7
	v_mbcnt_lo_u32_b32 v132, -1, 0
	v_mbcnt_hi_u32_b32 v132, -1, v132
	v_lshlrev_b32_e32 v132, 2, v132
	v_add_u32_e32 v132, 0x20080, v132
	ds_read_b32 v133, v132
	s_waitcnt lgkmcnt(0)
	v_cmp_ge_i32_e32 vcc, s2, v133
	s_nop 1
	s_and_b32 s3, vcc_lo, -2
	s_bcnt1_i32_b32 s3, s3
	v_mov_b32_e32 v181, s3
	v_lshlrev_b32_e32 v132, 2, v181
	v_add_u32_e32 v134, 0, v132
	v_add_u32_e32 v132, 0x20080, v134
	ds_read2_b32 v[132:133], v132 offset1:33
	v_add_u32_e32 v134, 0x20000, v134
	ds_read_b32 v134, v134
	s_waitcnt lgkmcnt(1)
	v_readfirstlane_b32 s3, v132
	s_sub_i32 s2, s2, s3
	s_lshl_b32 s77, s2, 8
	s_waitcnt lgkmcnt(0)
	v_readfirstlane_b32 s2, v134
	s_sub_i32 s2, s2, s77
	s_min_i32 s78, s2, 0x100
	v_readfirstlane_b32 s2, v133
	s_add_i32 s79, s2, s77
